# combo12 + out-proj epilogue: (address,data) records permuted through LDS so a lane quad stores 64 contiguous bytes; stores issued one block late, counted vmcnt ladder lowered by one
# speedup vs baseline: 1.0015x; 1.0015x over previous
.LBB0_754:
	s_mov_b32 s5, s61
	v_mbcnt_lo_u32_b32 v144, -1, 0
	v_mbcnt_hi_u32_b32 v144, -1, v144
	s_lshl_b32 s74, s61, 10
	v_and_b32_e32 v219, 15, v144
	s_add_i32 s74, s74, 0xc000
	v_lshrrev_b32_e32 v182, 4, v144
	v_bfe_u32 v184, v144, 1, 2
	v_xor_b32_e32 v182, v182, v184
	v_lshl_or_b32 v219, v219, 2, v182
	v_lshlrev_b32_e32 v219, 4, v219
	v_add_u32_e32 v219, s74, v219
	v_bfe_u32 v182, v144, 3, 2
	v_and_b32_e32 v184, 3, v144
	v_xor_b32_e32 v182, v182, v184
	v_lshrrev_b32_e32 v184, 2, v144
	v_lshl_or_b32 v184, v184, 2, v182
	v_lshlrev_b32_e32 v184, 4, v184
	v_add_u32_e32 v184, s74, v184
	s_lshl_b32 s19, s4, 8
	v_lshl_or_b32 v128, s5, 6, v144
	s_lshl_b32 s5, s24, 8
	v_readfirstlane_b32 s17, v128
	s_lshr_b32 s24, s17, 1
	s_and_b32 s24, s24, 0x60
	s_or_b32 s5, s24, s5
	v_lshrrev_b32_e32 v128, 1, v144
	s_ashr_i32 s4, s4, 3
	v_and_or_b32 v152, v128, 24, s5
	s_mul_hi_i32 s5, s4, 0x6000
	s_mulk_i32 s4, 0x6000
	s_add_u32 s4, s50, s4
	s_addc_u32 s5, s51, s5
	v_ashrrev_i32_e32 v153, 31, v152
	v_lshl_add_u64 v[132:133], v[152:153], 2, s[4:5]
	global_load_dwordx4 v[136:139], v[132:133], off offset:16
	global_load_dwordx4 v[140:143], v[132:133], off
	global_load_dwordx4 v[128:131], v[132:133], off offset:528
	s_nop 0
	global_load_dwordx4 v[132:135], v[132:133], off offset:512
	s_ashr_i32 s4, s17, 2
	s_andn2_b32 s4, s4, 63
	v_lshlrev_b32_e32 v145, 1, v144
	v_and_b32_e32 v145, 24, v145
	v_and_b32_e32 v144, 3, v144
	s_add_i32 s4, s4, s19
	v_or3_b32 v154, s4, v144, v145
	v_ashrrev_i32_e32 v155, 31, v154
	v_lshlrev_b64 v[144:145], 10, v[154:155]
	v_lshl_add_u64 v[156:157], v[144:145], 0, v[152:153]
	v_cndmask_b32_e64 v144, 0, 1, s[14:15]
	v_cmp_ne_u32_e64 s[4:5], 1, v144
	s_andn2_b64 vcc, exec, s[14:15]
	v_lshl_add_u64 v[158:159], v[156:157], 2, s[6:7]
	s_cbranch_vccnz .LBB0_805
	global_load_dwordx4 v[166:169], v[158:159], off offset:16
	global_load_dwordx4 v[170:173], v[158:159], off
	global_load_dwordx4 v[174:177], v[158:159], off offset:528
	global_load_dwordx4 v[178:181], v[158:159], off offset:512
	s_mov_b64 s[78:79], 0x4000
	v_lshl_add_u64 v[250:251], v[158:159], 0, s[78:79]
	global_load_dwordx4 v[186:189], v[250:251], off offset:16
	global_load_dwordx4 v[190:193], v[250:251], off
	global_load_dwordx4 v[194:197], v[250:251], off offset:528
	global_load_dwordx4 v[198:201], v[250:251], off offset:512
	s_mov_b64 s[78:79], 0x20000
	v_lshl_add_u64 v[248:249], v[158:159], 0, s[78:79]
	global_load_dwordx4 v[202:205], v[248:249], off offset:16
	global_load_dwordx4 v[206:209], v[248:249], off
	global_load_dwordx4 v[210:213], v[248:249], off offset:528
	global_load_dwordx4 v[214:217], v[248:249], off offset:512
	s_mov_b64 s[78:79], 0x24000
	v_lshl_add_u64 v[250:251], v[158:159], 0, s[78:79]
	global_load_dwordx4 v[228:231], v[250:251], off offset:16
	global_load_dwordx4 v[232:235], v[250:251], off
	global_load_dwordx4 v[236:239], v[250:251], off offset:528
	global_load_dwordx4 v[244:247], v[250:251], off offset:512
	s_waitcnt vmcnt(14)
	v_mov_b64_e32 v[148:149], v[166:167]
	v_mov_b64_e32 v[150:151], v[168:169]
	v_mov_b64_e32 v[144:145], v[170:171]
	v_mov_b64_e32 v[146:147], v[172:173]
	v_lshl_add_u64 v[156:157], v[156:157], 1, s[10:11]
	v_mov_b32_e32 v218, v183
	s_cbranch_execnz .LBB0_757

.LBB0_757:
	s_mov_b32 s24, 0x3b000000
	v_pk_mul_f32 v[140:141], v[140:141], s[24:25] op_sel_hi:[1,0]
	v_pk_mul_f32 v[138:139], v[138:139], s[24:25] op_sel_hi:[1,0]
	v_pk_mul_f32 v[136:137], v[136:137], s[24:25] op_sel_hi:[1,0]
	v_pk_mul_f32 v[142:143], v[142:143], s[24:25] op_sel_hi:[1,0]
	v_pk_fma_f32 v[124:125], v[124:125], v[140:141], v[144:145]
	v_pk_fma_f32 v[144:145], v[122:123], v[138:139], v[150:151]
	v_pk_fma_f32 v[122:123], v[120:121], v[136:137], v[148:149]
	s_and_b64 vcc, exec, s[4:5]
	v_pk_fma_f32 v[126:127], v[126:127], v[142:143], v[146:147]
	v_cvt_pk_bf16_f32 v120, v124, v125
	s_nop 0
	v_cvt_pk_bf16_f32 v121, v126, v127
	v_cvt_pk_bf16_f32 v122, v122, v123
	v_cvt_pk_bf16_f32 v123, v144, v145
	ds_write_b64 v219, v[156:157] offset:8192
	ds_write_b128 v219, v[120:123]
	ds_read_b64 v[224:225], v184 offset:8192
	ds_read_b128 v[220:223], v184
	s_cbranch_vccnz .LBB0_806
	s_waitcnt vmcnt(12)
	v_mov_b64_e32 v[124:125], v[174:175]
	v_mov_b64_e32 v[126:127], v[176:177]
	v_mov_b64_e32 v[120:121], v[178:179]
	v_mov_b64_e32 v[122:123], v[180:181]
	s_cbranch_execnz .LBB0_760
.LBB0_759:
	s_waitcnt vmcnt(14)
	v_lshlrev_b32_e32 v120, 16, v170
	v_and_b32_e32 v121, 0xffff0000, v170
	v_lshlrev_b32_e32 v122, 16, v171
	v_and_b32_e32 v123, 0xffff0000, v171
	v_lshlrev_b32_e32 v124, 16, v172
	v_and_b32_e32 v125, 0xffff0000, v172
	v_lshlrev_b32_e32 v126, 16, v173
	v_and_b32_e32 v127, 0xffff0000, v173
.LBB0_760:
	s_waitcnt lgkmcnt(0)
	global_store_dwordx4 v[224:225], v[220:223], off
	s_mov_b32 s24, 0x3b000000
	v_pk_mul_f32 v[132:133], v[132:133], s[24:25] op_sel_hi:[1,0]
	v_pk_mul_f32 v[130:131], v[130:131], s[24:25] op_sel_hi:[1,0]
	v_pk_mul_f32 v[128:129], v[128:129], s[24:25] op_sel_hi:[1,0]
	v_pk_mul_f32 v[134:135], v[134:135], s[24:25] op_sel_hi:[1,0]
	v_pk_fma_f32 v[116:117], v[116:117], v[132:133], v[120:121]
	v_pk_fma_f32 v[120:121], v[114:115], v[130:131], v[126:127]
	v_pk_fma_f32 v[114:115], v[112:113], v[128:129], v[124:125]
	v_cvt_pk_bf16_f32 v112, v116, v117
	v_pk_fma_f32 v[118:119], v[118:119], v[134:135], v[122:123]
	s_and_b64 vcc, exec, s[4:5]
	v_cvt_pk_bf16_f32 v113, v118, v119
	v_cvt_pk_bf16_f32 v114, v114, v115
	v_cvt_pk_bf16_f32 v115, v120, v121
	ds_write_b128 v219, v[112:115]
	ds_read_b128 v[240:243], v184
	s_nop 1
	v_or_b32_e32 v112, 4, v154
	v_ashrrev_i32_e32 v113, 31, v112
	v_lshlrev_b64 v[112:113], 10, v[112:113]
	v_lshl_add_u64 v[120:121], v[112:113], 0, v[152:153]
	v_lshl_add_u64 v[122:123], v[120:121], 2, s[6:7]
	s_cbranch_vccnz .LBB0_807
	s_waitcnt vmcnt(11)
	v_mov_b64_e32 v[116:117], v[186:187]
	v_mov_b64_e32 v[118:119], v[188:189]
	v_mov_b64_e32 v[112:113], v[190:191]
	v_mov_b64_e32 v[114:115], v[192:193]
	v_lshl_add_u64 v[120:121], v[120:121], 1, s[10:11]
	s_cbranch_execnz .LBB0_763
.LBB0_762:
	s_waitcnt vmcnt(14)
	v_lshlrev_b32_e32 v112, 16, v174
	v_and_b32_e32 v113, 0xffff0000, v174
	v_lshlrev_b32_e32 v114, 16, v175
	v_and_b32_e32 v115, 0xffff0000, v175
	v_lshlrev_b32_e32 v116, 16, v176
	v_and_b32_e32 v117, 0xffff0000, v176
	v_lshlrev_b32_e32 v118, 16, v177
	v_and_b32_e32 v119, 0xffff0000, v177
.LBB0_763:
	s_waitcnt lgkmcnt(0)
	global_store_dwordx4 v[224:225], v[240:243], off offset:256
	v_pk_fma_f32 v[108:109], v[108:109], v[140:141], v[112:113]
	v_pk_fma_f32 v[112:113], v[106:107], v[138:139], v[118:119]
	v_pk_fma_f32 v[106:107], v[104:105], v[136:137], v[116:117]
	s_and_b64 vcc, exec, s[4:5]
	v_pk_fma_f32 v[110:111], v[110:111], v[142:143], v[114:115]
	v_cvt_pk_bf16_f32 v104, v108, v109
	s_nop 0
	v_cvt_pk_bf16_f32 v105, v110, v111
	v_cvt_pk_bf16_f32 v106, v106, v107
	v_cvt_pk_bf16_f32 v107, v112, v113
	ds_write_b64 v219, v[120:121] offset:8192
	ds_write_b128 v219, v[104:107]
	ds_read_b64 v[224:225], v184 offset:8192
	ds_read_b128 v[220:223], v184
	s_cbranch_vccnz .LBB0_808
	s_waitcnt vmcnt(10)
	v_mov_b64_e32 v[108:109], v[194:195]
	v_mov_b64_e32 v[110:111], v[196:197]
	v_mov_b64_e32 v[104:105], v[198:199]
	v_mov_b64_e32 v[106:107], v[200:201]
	s_cbranch_execnz .LBB0_766
.LBB0_765:
	s_waitcnt vmcnt(14)
	v_lshlrev_b32_e32 v104, 16, v178
	v_and_b32_e32 v105, 0xffff0000, v178
	v_lshlrev_b32_e32 v106, 16, v179
	v_and_b32_e32 v107, 0xffff0000, v179
	v_lshlrev_b32_e32 v108, 16, v180
	v_and_b32_e32 v109, 0xffff0000, v180
	v_lshlrev_b32_e32 v110, 16, v181
	v_and_b32_e32 v111, 0xffff0000, v181
.LBB0_766:
	s_waitcnt lgkmcnt(0)
	global_store_dwordx4 v[224:225], v[220:223], off
	v_pk_fma_f32 v[100:101], v[100:101], v[132:133], v[104:105]
	v_pk_fma_f32 v[104:105], v[98:99], v[130:131], v[110:111]
	v_pk_fma_f32 v[98:99], v[96:97], v[128:129], v[108:109]
	v_cvt_pk_bf16_f32 v96, v100, v101
	v_pk_fma_f32 v[102:103], v[102:103], v[134:135], v[106:107]
	s_and_b64 vcc, exec, s[4:5]
	v_cvt_pk_bf16_f32 v97, v102, v103
	v_cvt_pk_bf16_f32 v98, v98, v99
	v_cvt_pk_bf16_f32 v99, v104, v105
	ds_write_b128 v219, v[96:99]
	ds_read_b128 v[240:243], v184
	s_nop 1
	v_or_b32_e32 v96, 32, v154
	v_ashrrev_i32_e32 v97, 31, v96
	v_lshlrev_b64 v[96:97], 10, v[96:97]
	v_lshl_add_u64 v[104:105], v[96:97], 0, v[152:153]
	v_lshl_add_u64 v[106:107], v[104:105], 2, s[6:7]
	s_cbranch_vccnz .LBB0_809
	s_waitcnt vmcnt(9)
	v_mov_b64_e32 v[100:101], v[202:203]
	v_mov_b64_e32 v[102:103], v[204:205]
	v_mov_b64_e32 v[96:97], v[206:207]
	v_mov_b64_e32 v[98:99], v[208:209]
	v_lshl_add_u64 v[104:105], v[104:105], 1, s[10:11]
	s_cbranch_execnz .LBB0_769
.LBB0_768:
	s_waitcnt vmcnt(14)
	v_lshlrev_b32_e32 v96, 16, v186
	v_and_b32_e32 v97, 0xffff0000, v186
	v_lshlrev_b32_e32 v98, 16, v187
	v_and_b32_e32 v99, 0xffff0000, v187
	v_lshlrev_b32_e32 v100, 16, v188
	v_and_b32_e32 v101, 0xffff0000, v188
	v_lshlrev_b32_e32 v102, 16, v189
	v_and_b32_e32 v103, 0xffff0000, v189
.LBB0_769:
	s_waitcnt lgkmcnt(0)
	global_store_dwordx4 v[224:225], v[240:243], off offset:256
	v_pk_fma_f32 v[92:93], v[92:93], v[140:141], v[96:97]
	v_pk_fma_f32 v[96:97], v[90:91], v[138:139], v[102:103]
	v_pk_fma_f32 v[90:91], v[88:89], v[136:137], v[100:101]
	s_and_b64 vcc, exec, s[4:5]
	v_pk_fma_f32 v[94:95], v[94:95], v[142:143], v[98:99]
	v_cvt_pk_bf16_f32 v88, v92, v93
	s_nop 0
	v_cvt_pk_bf16_f32 v89, v94, v95
	v_cvt_pk_bf16_f32 v90, v90, v91
	v_cvt_pk_bf16_f32 v91, v96, v97
	ds_write_b64 v219, v[104:105] offset:8192
	ds_write_b128 v219, v[88:91]
	ds_read_b64 v[224:225], v184 offset:8192
	ds_read_b128 v[220:223], v184
	s_cbranch_vccnz .LBB0_810
	s_waitcnt vmcnt(8)
	v_mov_b64_e32 v[92:93], v[210:211]
	v_mov_b64_e32 v[94:95], v[212:213]
	v_mov_b64_e32 v[88:89], v[214:215]
	v_mov_b64_e32 v[90:91], v[216:217]
	s_cbranch_execnz .LBB0_772
.LBB0_771:
	s_waitcnt vmcnt(14)
	v_lshlrev_b32_e32 v88, 16, v190
	v_and_b32_e32 v89, 0xffff0000, v190
	v_lshlrev_b32_e32 v90, 16, v191
	v_and_b32_e32 v91, 0xffff0000, v191
	v_lshlrev_b32_e32 v92, 16, v192
	v_and_b32_e32 v93, 0xffff0000, v192
	v_lshlrev_b32_e32 v94, 16, v193
	v_and_b32_e32 v95, 0xffff0000, v193
.LBB0_772:
	s_waitcnt lgkmcnt(0)
	global_store_dwordx4 v[224:225], v[220:223], off
	v_pk_fma_f32 v[84:85], v[84:85], v[132:133], v[88:89]
	v_pk_fma_f32 v[88:89], v[82:83], v[130:131], v[94:95]
	v_pk_fma_f32 v[82:83], v[80:81], v[128:129], v[92:93]
	v_cvt_pk_bf16_f32 v80, v84, v85
	v_pk_fma_f32 v[86:87], v[86:87], v[134:135], v[90:91]
	s_and_b64 vcc, exec, s[4:5]
	v_cvt_pk_bf16_f32 v81, v86, v87
	v_cvt_pk_bf16_f32 v82, v82, v83
	v_cvt_pk_bf16_f32 v83, v88, v89
	ds_write_b128 v219, v[80:83]
	ds_read_b128 v[240:243], v184
	s_nop 1
	v_or_b32_e32 v80, 36, v154
	v_ashrrev_i32_e32 v81, 31, v80
	v_lshlrev_b64 v[80:81], 10, v[80:81]
	v_lshl_add_u64 v[88:89], v[80:81], 0, v[152:153]
	v_lshl_add_u64 v[90:91], v[88:89], 2, s[6:7]
	s_cbranch_vccnz .LBB0_811
	s_waitcnt vmcnt(7)
	v_mov_b64_e32 v[84:85], v[228:229]
	v_mov_b64_e32 v[86:87], v[230:231]
	v_mov_b64_e32 v[80:81], v[232:233]
	v_mov_b64_e32 v[82:83], v[234:235]
	v_lshl_add_u64 v[88:89], v[88:89], 1, s[10:11]
	s_cbranch_execnz .LBB0_775
.LBB0_774:
	s_waitcnt vmcnt(14)
	v_lshlrev_b32_e32 v80, 16, v194
	v_and_b32_e32 v81, 0xffff0000, v194
	v_lshlrev_b32_e32 v82, 16, v195
	v_and_b32_e32 v83, 0xffff0000, v195
	v_lshlrev_b32_e32 v84, 16, v196
	v_and_b32_e32 v85, 0xffff0000, v196
	v_lshlrev_b32_e32 v86, 16, v197
	v_and_b32_e32 v87, 0xffff0000, v197
.LBB0_775:
	s_waitcnt lgkmcnt(0)
	global_store_dwordx4 v[224:225], v[240:243], off offset:256
	v_pk_fma_f32 v[76:77], v[76:77], v[140:141], v[80:81]
	v_pk_fma_f32 v[80:81], v[74:75], v[138:139], v[86:87]
	v_pk_fma_f32 v[74:75], v[72:73], v[136:137], v[84:85]
	s_and_b64 vcc, exec, s[4:5]
	v_pk_fma_f32 v[78:79], v[78:79], v[142:143], v[82:83]
	v_cvt_pk_bf16_f32 v72, v76, v77
	s_nop 0
	v_cvt_pk_bf16_f32 v73, v78, v79
	v_cvt_pk_bf16_f32 v74, v74, v75
	v_cvt_pk_bf16_f32 v75, v80, v81
	ds_write_b64 v219, v[88:89] offset:8192
	ds_write_b128 v219, v[72:75]
	ds_read_b64 v[224:225], v184 offset:8192
	ds_read_b128 v[220:223], v184
	s_cbranch_vccnz .LBB0_812
	s_waitcnt vmcnt(6)
	v_mov_b64_e32 v[76:77], v[236:237]
	v_mov_b64_e32 v[78:79], v[238:239]
	v_mov_b64_e32 v[72:73], v[244:245]
	v_mov_b64_e32 v[74:75], v[246:247]
	s_cbranch_execnz .LBB0_778
.LBB0_777:
	s_waitcnt vmcnt(14)
	v_lshlrev_b32_e32 v72, 16, v198
	v_and_b32_e32 v73, 0xffff0000, v198
	v_lshlrev_b32_e32 v74, 16, v199
	v_and_b32_e32 v75, 0xffff0000, v199
	v_lshlrev_b32_e32 v76, 16, v200
	v_and_b32_e32 v77, 0xffff0000, v200
	v_lshlrev_b32_e32 v78, 16, v201
	v_and_b32_e32 v79, 0xffff0000, v201
.LBB0_778:
	s_waitcnt lgkmcnt(0)
	global_store_dwordx4 v[224:225], v[220:223], off
	v_pk_fma_f32 v[68:69], v[68:69], v[132:133], v[72:73]
	v_pk_fma_f32 v[72:73], v[66:67], v[130:131], v[78:79]
	v_pk_fma_f32 v[66:67], v[64:65], v[128:129], v[76:77]
	v_pk_fma_f32 v[70:71], v[70:71], v[134:135], v[74:75]
	v_cvt_pk_bf16_f32 v64, v68, v69
	s_and_b64 vcc, exec, s[4:5]
	v_cvt_pk_bf16_f32 v65, v70, v71
	v_cvt_pk_bf16_f32 v66, v66, v67
	v_cvt_pk_bf16_f32 v67, v72, v73
	v_add_u32_e32 v72, 0x80, v154
	v_ashrrev_i32_e32 v73, 31, v72
	ds_write_b128 v219, v[64:67]
	ds_read_b128 v[240:243], v184
	s_nop 1
	v_lshlrev_b64 v[64:65], 10, v[72:73]
	v_lshl_add_u64 v[74:75], v[64:65], 0, v[152:153]
	v_lshl_add_u64 v[76:77], v[74:75], 2, s[6:7]
	s_cbranch_vccnz .LBB0_813
	s_mov_b64 s[78:79], 0x80000
	v_lshl_add_u64 v[248:249], v[158:159], 0, s[78:79]
	global_load_dwordx4 v[166:169], v[248:249], off offset:16
	global_load_dwordx4 v[170:173], v[248:249], off
	global_load_dwordx4 v[174:177], v[248:249], off offset:528
	global_load_dwordx4 v[178:181], v[248:249], off offset:512
	s_mov_b64 s[78:79], 0x84000
	v_lshl_add_u64 v[250:251], v[158:159], 0, s[78:79]
	global_load_dwordx4 v[186:189], v[250:251], off offset:16
	global_load_dwordx4 v[190:193], v[250:251], off
	global_load_dwordx4 v[194:197], v[250:251], off offset:528
	global_load_dwordx4 v[198:201], v[250:251], off offset:512
	s_mov_b64 s[78:79], 0xa0000
	v_lshl_add_u64 v[248:249], v[158:159], 0, s[78:79]
	global_load_dwordx4 v[202:205], v[248:249], off offset:16
	global_load_dwordx4 v[206:209], v[248:249], off
	global_load_dwordx4 v[210:213], v[248:249], off offset:528
	global_load_dwordx4 v[214:217], v[248:249], off offset:512
	s_mov_b64 s[78:79], 0xa4000
	v_lshl_add_u64 v[250:251], v[158:159], 0, s[78:79]
	global_load_dwordx4 v[228:231], v[250:251], off offset:16
	global_load_dwordx4 v[232:235], v[250:251], off
	global_load_dwordx4 v[236:239], v[250:251], off offset:528
	global_load_dwordx4 v[244:247], v[250:251], off offset:512
	s_waitcnt vmcnt(14)
	v_mov_b64_e32 v[68:69], v[166:167]
	v_mov_b64_e32 v[70:71], v[168:169]
	v_mov_b64_e32 v[64:65], v[170:171]
	v_mov_b64_e32 v[66:67], v[172:173]
	v_lshl_add_u64 v[74:75], v[74:75], 1, s[10:11]
	s_cbranch_execnz .LBB0_781
.LBB0_780:
	s_waitcnt vmcnt(14)
	v_lshlrev_b32_e32 v64, 16, v202
	v_and_b32_e32 v65, 0xffff0000, v202
	v_lshlrev_b32_e32 v66, 16, v203
	v_and_b32_e32 v67, 0xffff0000, v203
	v_lshlrev_b32_e32 v68, 16, v204
	v_and_b32_e32 v69, 0xffff0000, v204
	v_lshlrev_b32_e32 v70, 16, v205
	v_and_b32_e32 v71, 0xffff0000, v205
.LBB0_781:
	s_waitcnt lgkmcnt(0)
	global_store_dwordx4 v[224:225], v[240:243], off offset:256
	v_pk_fma_f32 v[60:61], v[60:61], v[140:141], v[64:65]
	v_pk_fma_f32 v[64:65], v[58:59], v[138:139], v[70:71]
	v_pk_fma_f32 v[58:59], v[56:57], v[136:137], v[68:69]
	s_and_b64 vcc, exec, s[4:5]
	v_pk_fma_f32 v[62:63], v[62:63], v[142:143], v[66:67]
	v_cvt_pk_bf16_f32 v56, v60, v61
	s_nop 0
	v_cvt_pk_bf16_f32 v57, v62, v63
	v_cvt_pk_bf16_f32 v58, v58, v59
	v_cvt_pk_bf16_f32 v59, v64, v65
	ds_write_b64 v219, v[74:75] offset:8192
	ds_write_b128 v219, v[56:59]
	ds_read_b64 v[224:225], v184 offset:8192
	ds_read_b128 v[220:223], v184
	s_cbranch_vccnz .LBB0_814
	s_waitcnt vmcnt(12)
	v_mov_b64_e32 v[60:61], v[174:175]
	v_mov_b64_e32 v[62:63], v[176:177]
	v_mov_b64_e32 v[56:57], v[178:179]
	v_mov_b64_e32 v[58:59], v[180:181]
	s_cbranch_execnz .LBB0_784
.LBB0_783:
	s_waitcnt vmcnt(14)
	v_lshlrev_b32_e32 v56, 16, v206
	v_and_b32_e32 v57, 0xffff0000, v206
	v_lshlrev_b32_e32 v58, 16, v207
	v_and_b32_e32 v59, 0xffff0000, v207
	v_lshlrev_b32_e32 v60, 16, v208
	v_and_b32_e32 v61, 0xffff0000, v208
	v_lshlrev_b32_e32 v62, 16, v209
	v_and_b32_e32 v63, 0xffff0000, v209
.LBB0_784:
	s_waitcnt lgkmcnt(0)
	global_store_dwordx4 v[224:225], v[220:223], off
	v_pk_fma_f32 v[52:53], v[52:53], v[132:133], v[56:57]
	v_pk_fma_f32 v[56:57], v[50:51], v[130:131], v[62:63]
	v_pk_fma_f32 v[50:51], v[48:49], v[128:129], v[60:61]
	v_cvt_pk_bf16_f32 v48, v52, v53
	v_pk_fma_f32 v[54:55], v[54:55], v[134:135], v[58:59]
	s_and_b64 vcc, exec, s[4:5]
	v_cvt_pk_bf16_f32 v49, v54, v55
	v_cvt_pk_bf16_f32 v50, v50, v51
	v_cvt_pk_bf16_f32 v51, v56, v57
	ds_write_b128 v219, v[48:51]
	ds_read_b128 v[240:243], v184
	s_nop 1
	v_or_b32_e32 v48, 4, v72
	v_ashrrev_i32_e32 v49, 31, v48
	v_lshlrev_b64 v[48:49], 10, v[48:49]
	v_lshl_add_u64 v[56:57], v[48:49], 0, v[152:153]
	v_lshl_add_u64 v[58:59], v[56:57], 2, s[6:7]
	s_cbranch_vccnz .LBB0_815
	s_waitcnt vmcnt(11)
	v_mov_b64_e32 v[52:53], v[186:187]
	v_mov_b64_e32 v[54:55], v[188:189]
	v_mov_b64_e32 v[48:49], v[190:191]
	v_mov_b64_e32 v[50:51], v[192:193]
	v_lshl_add_u64 v[56:57], v[56:57], 1, s[10:11]
	s_cbranch_execnz .LBB0_787
.LBB0_786:
	s_waitcnt vmcnt(14)
	v_lshlrev_b32_e32 v48, 16, v210
	v_and_b32_e32 v49, 0xffff0000, v210
	v_lshlrev_b32_e32 v50, 16, v211
	v_and_b32_e32 v51, 0xffff0000, v211
	v_lshlrev_b32_e32 v52, 16, v212
	v_and_b32_e32 v53, 0xffff0000, v212
	v_lshlrev_b32_e32 v54, 16, v213
	v_and_b32_e32 v55, 0xffff0000, v213
.LBB0_787:
	s_waitcnt lgkmcnt(0)
	global_store_dwordx4 v[224:225], v[240:243], off offset:256
	v_pk_fma_f32 v[44:45], v[44:45], v[140:141], v[48:49]
	v_pk_fma_f32 v[48:49], v[42:43], v[138:139], v[54:55]
	v_pk_fma_f32 v[42:43], v[40:41], v[136:137], v[52:53]
	s_and_b64 vcc, exec, s[4:5]
	v_pk_fma_f32 v[46:47], v[46:47], v[142:143], v[50:51]
	v_cvt_pk_bf16_f32 v40, v44, v45
	s_nop 0
	v_cvt_pk_bf16_f32 v41, v46, v47
	v_cvt_pk_bf16_f32 v42, v42, v43
	v_cvt_pk_bf16_f32 v43, v48, v49
	ds_write_b64 v219, v[56:57] offset:8192
	ds_write_b128 v219, v[40:43]
	ds_read_b64 v[224:225], v184 offset:8192
	ds_read_b128 v[220:223], v184
	s_cbranch_vccnz .LBB0_816
	s_waitcnt vmcnt(10)
	v_mov_b64_e32 v[44:45], v[194:195]
	v_mov_b64_e32 v[46:47], v[196:197]
	v_mov_b64_e32 v[40:41], v[198:199]
	v_mov_b64_e32 v[42:43], v[200:201]
	s_cbranch_execnz .LBB0_790
.LBB0_789:
	s_waitcnt vmcnt(14)
	v_lshlrev_b32_e32 v40, 16, v214
	v_and_b32_e32 v41, 0xffff0000, v214
	v_lshlrev_b32_e32 v42, 16, v215
	v_and_b32_e32 v43, 0xffff0000, v215
	v_lshlrev_b32_e32 v44, 16, v216
	v_and_b32_e32 v45, 0xffff0000, v216
	v_lshlrev_b32_e32 v46, 16, v217
	v_and_b32_e32 v47, 0xffff0000, v217
.LBB0_790:
	s_waitcnt lgkmcnt(0)
	global_store_dwordx4 v[224:225], v[220:223], off
	v_pk_fma_f32 v[36:37], v[36:37], v[132:133], v[40:41]
	v_pk_fma_f32 v[40:41], v[34:35], v[130:131], v[46:47]
	v_pk_fma_f32 v[34:35], v[32:33], v[128:129], v[44:45]
	v_cvt_pk_bf16_f32 v32, v36, v37
	v_pk_fma_f32 v[38:39], v[38:39], v[134:135], v[42:43]
	s_and_b64 vcc, exec, s[4:5]
	v_cvt_pk_bf16_f32 v33, v38, v39
	v_cvt_pk_bf16_f32 v34, v34, v35
	v_cvt_pk_bf16_f32 v35, v40, v41
	ds_write_b128 v219, v[32:35]
	ds_read_b128 v[240:243], v184
	s_nop 1
	v_or_b32_e32 v32, 32, v72
	v_ashrrev_i32_e32 v33, 31, v32
	v_lshlrev_b64 v[32:33], 10, v[32:33]
	v_lshl_add_u64 v[40:41], v[32:33], 0, v[152:153]
	v_lshl_add_u64 v[42:43], v[40:41], 2, s[6:7]
	s_cbranch_vccnz .LBB0_817
	s_waitcnt vmcnt(9)
	v_mov_b64_e32 v[36:37], v[202:203]
	v_mov_b64_e32 v[38:39], v[204:205]
	v_mov_b64_e32 v[32:33], v[206:207]
	v_mov_b64_e32 v[34:35], v[208:209]
	v_lshl_add_u64 v[40:41], v[40:41], 1, s[10:11]
	s_cbranch_execnz .LBB0_793
.LBB0_792:
	s_waitcnt vmcnt(14)
	v_lshlrev_b32_e32 v32, 16, v228
	v_and_b32_e32 v33, 0xffff0000, v228
	v_lshlrev_b32_e32 v34, 16, v229
	v_and_b32_e32 v35, 0xffff0000, v229
	v_lshlrev_b32_e32 v36, 16, v230
	v_and_b32_e32 v37, 0xffff0000, v230
	v_lshlrev_b32_e32 v38, 16, v231
	v_and_b32_e32 v39, 0xffff0000, v231
.LBB0_793:
	s_waitcnt lgkmcnt(0)
	global_store_dwordx4 v[224:225], v[240:243], off offset:256
	v_pk_fma_f32 v[28:29], v[28:29], v[140:141], v[32:33]
	v_pk_fma_f32 v[32:33], v[26:27], v[138:139], v[38:39]
	v_pk_fma_f32 v[26:27], v[24:25], v[136:137], v[36:37]
	s_and_b64 vcc, exec, s[4:5]
	v_pk_fma_f32 v[30:31], v[30:31], v[142:143], v[34:35]
	v_cvt_pk_bf16_f32 v24, v28, v29
	s_nop 0
	v_cvt_pk_bf16_f32 v25, v30, v31
	v_cvt_pk_bf16_f32 v26, v26, v27
	v_cvt_pk_bf16_f32 v27, v32, v33
	ds_write_b64 v219, v[40:41] offset:8192
	ds_write_b128 v219, v[24:27]
	ds_read_b64 v[224:225], v184 offset:8192
	ds_read_b128 v[220:223], v184
	s_cbranch_vccnz .LBB0_818
	s_waitcnt vmcnt(8)
	v_mov_b64_e32 v[28:29], v[210:211]
	v_mov_b64_e32 v[30:31], v[212:213]
	v_mov_b64_e32 v[24:25], v[214:215]
	v_mov_b64_e32 v[26:27], v[216:217]
	s_cbranch_execnz .LBB0_796
.LBB0_795:
	s_waitcnt vmcnt(14)
	v_lshlrev_b32_e32 v24, 16, v232
	v_and_b32_e32 v25, 0xffff0000, v232
	v_lshlrev_b32_e32 v26, 16, v233
	v_and_b32_e32 v27, 0xffff0000, v233
	v_lshlrev_b32_e32 v28, 16, v234
	v_and_b32_e32 v29, 0xffff0000, v234
	v_lshlrev_b32_e32 v30, 16, v235
	v_and_b32_e32 v31, 0xffff0000, v235
.LBB0_796:
	s_waitcnt lgkmcnt(0)
	global_store_dwordx4 v[224:225], v[220:223], off
	v_pk_fma_f32 v[20:21], v[20:21], v[132:133], v[24:25]
	v_pk_fma_f32 v[24:25], v[18:19], v[130:131], v[30:31]
	v_pk_fma_f32 v[18:19], v[16:17], v[128:129], v[28:29]
	v_cvt_pk_bf16_f32 v16, v20, v21
	v_pk_fma_f32 v[22:23], v[22:23], v[134:135], v[26:27]
	s_and_b64 vcc, exec, s[4:5]
	v_cvt_pk_bf16_f32 v17, v22, v23
	v_cvt_pk_bf16_f32 v18, v18, v19
	v_cvt_pk_bf16_f32 v19, v24, v25
	ds_write_b128 v219, v[16:19]
	ds_read_b128 v[240:243], v184
	s_nop 1
	v_or_b32_e32 v16, 36, v72
	v_ashrrev_i32_e32 v17, 31, v16
	v_lshlrev_b64 v[16:17], 10, v[16:17]
	v_lshl_add_u64 v[24:25], v[16:17], 0, v[152:153]
	v_lshl_add_u64 v[26:27], v[24:25], 2, s[6:7]
	s_cbranch_vccnz .LBB0_819
	s_waitcnt vmcnt(7)
	v_mov_b64_e32 v[20:21], v[228:229]
	v_mov_b64_e32 v[22:23], v[230:231]
	v_mov_b64_e32 v[16:17], v[232:233]
	v_mov_b64_e32 v[18:19], v[234:235]
	v_lshl_add_u64 v[24:25], v[24:25], 1, s[10:11]
	s_cbranch_execnz .LBB0_799
.LBB0_798:
	s_waitcnt vmcnt(14)
	v_lshlrev_b32_e32 v16, 16, v236
	v_and_b32_e32 v17, 0xffff0000, v236
	v_lshlrev_b32_e32 v18, 16, v237
	v_and_b32_e32 v19, 0xffff0000, v237
	v_lshlrev_b32_e32 v20, 16, v238
	v_and_b32_e32 v21, 0xffff0000, v238
	v_lshlrev_b32_e32 v22, 16, v239
	v_and_b32_e32 v23, 0xffff0000, v239
.LBB0_799:
	s_waitcnt lgkmcnt(0)
	global_store_dwordx4 v[224:225], v[240:243], off offset:256
	v_pk_fma_f32 v[12:13], v[12:13], v[140:141], v[16:17]
	v_pk_fma_f32 v[16:17], v[10:11], v[138:139], v[22:23]
	v_pk_fma_f32 v[10:11], v[8:9], v[136:137], v[20:21]
	s_and_b64 vcc, exec, s[4:5]
	v_pk_fma_f32 v[14:15], v[14:15], v[142:143], v[18:19]
	v_cvt_pk_bf16_f32 v8, v12, v13
	s_nop 0
	v_cvt_pk_bf16_f32 v9, v14, v15
	v_cvt_pk_bf16_f32 v10, v10, v11
	v_cvt_pk_bf16_f32 v11, v16, v17
	ds_write_b64 v219, v[24:25] offset:8192
	ds_write_b128 v219, v[8:11]
	ds_read_b64 v[224:225], v184 offset:8192
	ds_read_b128 v[220:223], v184
	s_cbranch_vccnz .LBB0_820
	s_waitcnt vmcnt(6)
	v_mov_b64_e32 v[12:13], v[236:237]
	v_mov_b64_e32 v[14:15], v[238:239]
	v_mov_b64_e32 v[8:9], v[244:245]
	v_mov_b64_e32 v[10:11], v[246:247]
	s_cbranch_execnz .LBB0_802
.LBB0_801:
	s_waitcnt vmcnt(14)
	v_lshlrev_b32_e32 v8, 16, v244
	v_and_b32_e32 v9, 0xffff0000, v244
	v_lshlrev_b32_e32 v10, 16, v245
	v_and_b32_e32 v11, 0xffff0000, v245
	v_lshlrev_b32_e32 v12, 16, v246
	v_and_b32_e32 v13, 0xffff0000, v246
	v_lshlrev_b32_e32 v14, 16, v247
	v_and_b32_e32 v15, 0xffff0000, v247
.LBB0_802:
	s_waitcnt lgkmcnt(0)
	global_store_dwordx4 v[224:225], v[220:223], off
	v_pk_fma_f32 v[4:5], v[4:5], v[132:133], v[8:9]
	v_pk_fma_f32 v[8:9], v[2:3], v[130:131], v[14:15]
	v_pk_fma_f32 v[2:3], v[0:1], v[128:129], v[12:13]
	v_pk_fma_f32 v[6:7], v[6:7], v[134:135], v[10:11]
	v_cvt_pk_bf16_f32 v0, v4, v5
	s_andn2_b64 vcc, exec, s[2:3]
	v_cvt_pk_bf16_f32 v1, v6, v7
	v_cvt_pk_bf16_f32 v2, v2, v3
	v_cvt_pk_bf16_f32 v3, v8, v9
	s_mov_b64 s[2:3], -1
	ds_write_b128 v219, v[0:3]
	ds_read_b128 v[240:243], v184
	s_waitcnt lgkmcnt(0)
	global_store_dwordx4 v[224:225], v[240:243], off offset:256
	s_cbranch_vccnz .LBB0_743
	s_nop 0
	v_mov_b32_e32 v0, v185
	s_andn2_b64 vcc, exec, s[8:9]
	s_cbranch_vccnz .LBB0_742
	s_barrier
	s_branch .LBB0_742
